# MoE-phase helpers use the pair4 mapping (waves w and w+4 write the two 64-byte halves of each output line at the same time) with nt stores
# speedup vs baseline: 1.0063x; 1.0063x over previous
; #define LAS __attribute__((address_space(3)))
;     ...
;         LAS float* scr = (LAS float*)(lds + wave * 16640);
;         const int gw = vcu * NWAVES + wave, NGW = G * NWAVES;
;         constexpr int C_IN = 32 * 188, C_OA = 8 * 32, C_OB = 16 * 32, C_O = 32 * 32, C_GU = 16 * 32 * 32, C_DN = 16 * 16 * 32, C_L = C_IN + C_OA + C_OB + C_O + C_GU + C_DN, NIT = DEPTH * C_L;
;         const int q4 = lane & 15, kk = lane >> 4;
;         auto decode = [&](int it) -> TrDesc {
;             TrDesc d; d.zero = 0; d.rope = 0; d.f8 = 0;
;             const int l = it / C_L; int r = it % C_L;
;             const float* W; unsigned char* WT; int ldw, K, k0, n0, scol, esz = 2;
;             if (r < C_IN) { const int kb = r / 188, nb = r % 188; n0 = 64 * nb; k0 = 64 * kb; ldw = NIN; K = D; W = a.w_in + (size_t)l * D * NIN;
;                 if (n0 < 3072) { d.rope = 1; scol = (n0 >> 7) * 128 + 32 * ((n0 >> 6) & 1) + 64 * (q4 >> 3) + 4 * (q4 & 7); }
;                 else if (n0 < 7680) scol = n0 + 4 * q4;
;                 else if (n0 < 11776) scol = n0 + 16 + 4 * q4;
;                 else if (n0 == 11776) { scol = (q4 < 4) ? 7680 + 4 * q4 : 0; d.zero = (q4 < 4) ? 0 : 1; }
;                 else { scol = 0; d.zero = 1; }
;     ...
;                 d.f8 = 1; esz = 1; WT = ws + WS_WIN + (size_t)l * NP * D;
;     ...
;                 WT = ws + WS_WIN + (size_t)l * NP * D * 2;
;     ...
;             } else if ((r -= C_IN) < C_OA) { const int kb = r / 32, nb = r % 32; n0 = 64 * nb; k0 = 64 * kb; ldw = D; K = 512; scol = n0 + 4 * q4; W = a.w_out_a + (size_t)l * 512 * D; WT = ws + WS_WOA + (size_t)l * D * 512 * (MIX_F8 ? 1 : 2); if (MIX_F8) { d.f8 = 1; esz = 1; }
;                 if (BR_FUSE) { K = 1536; WT = ws + WS_WOA + (size_t)l * D * 1536 + 1024; }
;             } else if ((r -= C_OA) < C_OB) { const int kb = r / 32, nb = r % 32; n0 = 64 * nb; k0 = 64 * kb; ldw = D; K = 1024; scol = n0 + 4 * q4; W = a.w_out_b + (size_t)l * 1024 * D; WT = ws + WS_WOB + (size_t)l * D * 1024 * (MIX_F8 ? 1 : 2); if (MIX_F8) { d.f8 = 1; esz = 1; }
;                 if (BR_FUSE) { K = 1536; WT = ws + WS_WOA + (size_t)l * D * 1536; }
;             } else if ((r -= C_OB) < C_O) { const int kb = r / 32, nb = r % 32; n0 = 64 * nb; k0 = 64 * kb; ldw = D; K = D; scol = n0 + 4 * q4; W = a.w_out + (size_t)l * D * D; WT = ws + WS_WO + (size_t)l * D * D * (MIX_F8 ? 1 : 2); if (MIX_F8) { d.f8 = 1; esz = 1; }
.Lhp_entry:
	v_writelane_b32 v251, s16, 0
	v_writelane_b32 v251, s17, 1
	v_writelane_b32 v251, s18, 2
	v_writelane_b32 v251, s19, 3
	v_writelane_b32 v251, s20, 4
	v_writelane_b32 v251, s21, 5
	v_writelane_b32 v251, s23, 6
	v_writelane_b32 v251, s25, 7
	v_writelane_b32 v251, s26, 8
	v_writelane_b32 v251, s33, 9
	v_writelane_b32 v251, s38, 10
	v_writelane_b32 v251, s39, 11
	v_writelane_b32 v251, s41, 12
	v_writelane_b32 v251, s42, 13
	v_writelane_b32 v251, s45, 14
	v_writelane_b32 v251, s48, 15
	v_writelane_b32 v251, s49, 16
	v_writelane_b32 v251, s50, 17
	v_writelane_b32 v251, s51, 18
	v_writelane_b32 v251, s74, 19
	v_writelane_b32 v251, s76, 20
	v_mov_b32_e32 v193, v3
	v_mov_b32_e32 v194, v33
	v_mov_b32_e32 v195, v59
	v_mov_b32_e32 v196, v63
	v_mov_b32_e32 v197, v110
	v_mov_b32_e32 v198, v111
	v_mov_b32_e32 v199, v114
	v_mov_b32_e32 v200, v115
	v_mov_b32_e32 v201, v149
	v_mov_b32_e32 v202, v153
	v_mov_b32_e32 v203, v157
	v_mov_b32_e32 v204, v161
	v_mov_b32_e32 v205, v165
	v_mov_b32_e32 v206, v169
	v_mov_b32_e32 v207, v173
	v_mov_b32_e32 v208, v177
	v_mov_b32_e32 v209, v178
	v_mov_b32_e32 v210, v179
	v_mov_b32_e32 v211, v180
	v_mov_b32_e32 v212, v181
	v_mov_b32_e32 v214, v182
	v_mov_b32_e32 v215, v183
	v_mov_b32_e32 v216, v184
	v_mov_b32_e32 v218, v185
	s_mov_b32 s74, s0
	v_readlane_b32 s76, v253, 4
	v_readlane_b32 s8, v253, 0
	v_readlane_b32 s9, v253, 1
	s_nop 1
	s_add_i32 s0, s76, s74
	s_sub_i32 s0, s0, 0x100
	s_lshr_b32 s1, s100, 3
	s_add_i32 s0, s0, s1
	s_lshr_b32 s33, s78, 6
	s_lshr_b32 s1, s0, 3
	s_lshl_b32 s1, s1, 6
	s_and_b32 s0, s0, 7
	s_lshl_b32 s0, s0, 2
	s_or_b32 s1, s1, s0
	s_and_b32 s0, s33, 3
	s_or_b32 s1, s1, s0
	s_lshr_b32 s0, s33, 2
	s_lshl_b32 s0, s0, 5
	s_or_b32 s1, s1, s0
	s_sub_i32 s100, s1, s33
	s_mov_b32 s76, 0
	s_load_dwordx2 s[10:11], s[8:9], 0xa0
	v_mbcnt_lo_u32_b32 v69, -1, 0
	v_mbcnt_hi_u32_b32 v69, -1, v69
	s_mov_b64 exec, -1
	v_lshlrev_b32_e32 v76, 3, v69
	s_waitcnt lgkmcnt(0)
	s_lshl_b32 s47, s76, 3
	s_add_i32 s47, s47, s33
	s_add_i32 s47, s47, s100
	v_and_b32_e32 v2, 15, v69
	s_cmp_ge_i32 s47, s101
	v_ashrrev_i32_e32 v133, 4, v69
	s_cbranch_scc1 .LBB0_36_hp
	s_sub_i32 s1, 0xfcff, s47
	s_mul_hi_u32 s0, s1, 0x81848da9
	s_lshr_b32 s0, s0, 14
	s_mul_i32 s2, s0, 0x7e80
	s_sub_i32 s17, s1, s2
	s_cmpk_gt_u32 s17, 0x177f
	s_cbranch_scc0 .LBB0_37_hp
	s_cmpk_gt_u32 s17, 0x187f
	s_cbranch_scc0 .LBB0_39_hp
	s_cmpk_gt_u32 s17, 0x1a7f
	s_cbranch_scc0 .LBB0_40_hp
	s_cmpk_gt_u32 s17, 0x1e7f
	s_cbranch_scc0 .LBB0_41_hp
	s_lshl_b32 s1, s17, 6
	s_cmpk_gt_u32 s17, 0x5e7f
	s_cbranch_scc0 .LBB0_42_hp
	s_add_i32 s2, s17, 0xffffa180
	s_lshr_b32 s4, s2, 9
	s_lshl_b32 s2, s2, 1
	s_and_b32 s18, s2, 0x3c0
	s_load_dwordx2 s[2:3], s[8:9], 0x88
	s_lshl_b32 s5, s0, 4
	s_add_i32 s6, s4, s5
	s_mov_b32 s7, 0
	s_and_b32 s16, s1, 0x7c0
	s_lshl_b64 s[4:5], s[6:7], 23
	s_waitcnt lgkmcnt(0)
	s_add_u32 s4, s2, s4
	s_addc_u32 s5, s3, s5
	s_lshl_b64 s[2:3], s[6:7], 21
	s_add_u32 s2, s10, s2
	s_addc_u32 s3, s11, s3
	s_add_u32 s6, s2, 0x18600000
	v_lshl_or_b32 v0, v2, 2, s16
	s_addc_u32 s7, s3, 0
	s_mov_b64 s[2:3], 0
	s_branch .LBB0_43_hp

;     ...
;         auto decode = [&](int it) -> TrDesc {
;             TrDesc d; d.zero = 0; d.rope = 0; d.f8 = 0;
;             const int l = it / C_L; int r = it % C_L;
;             const float* W; unsigned char* WT; int ldw, K, k0, n0, scol, esz = 2;
;             if (r < C_IN) { const int kb = r / 188, nb = r % 188; n0 = 64 * nb; k0 = 64 * kb; ldw = NIN; K = D; W = a.w_in + (size_t)l * D * NIN;
;                 if (n0 < 3072) { d.rope = 1; scol = (n0 >> 7) * 128 + 32 * ((n0 >> 6) & 1) + 64 * (q4 >> 3) + 4 * (q4 & 7); }
;                 else if (n0 < 7680) scol = n0 + 4 * q4;
;                 else if (n0 < 11776) scol = n0 + 16 + 4 * q4;
;                 else if (n0 == 11776) { scol = (q4 < 4) ? 7680 + 4 * q4 : 0; d.zero = (q4 < 4) ? 0 : 1; }
;                 else { scol = 0; d.zero = 1; }
;     ...
;                 d.f8 = 1; esz = 1; WT = ws + WS_WIN + (size_t)l * NP * D;
;     ...
;                 WT = ws + WS_WIN + (size_t)l * NP * D * 2;
;     ...
;             } else if ((r -= C_IN) < C_OA) { const int kb = r / 32, nb = r % 32; n0 = 64 * nb; k0 = 64 * kb; ldw = D; K = 512; scol = n0 + 4 * q4; W = a.w_out_a + (size_t)l * 512 * D; WT = ws + WS_WOA + (size_t)l * D * 512 * (MIX_F8 ? 1 : 2); if (MIX_F8) { d.f8 = 1; esz = 1; }
;                 if (BR_FUSE) { K = 1536; WT = ws + WS_WOA + (size_t)l * D * 1536 + 1024; }
;             } else if ((r -= C_OA) < C_OB) { const int kb = r / 32, nb = r % 32; n0 = 64 * nb; k0 = 64 * kb; ldw = D; K = 1024; scol = n0 + 4 * q4; W = a.w_out_b + (size_t)l * 1024 * D; WT = ws + WS_WOB + (size_t)l * D * 1024 * (MIX_F8 ? 1 : 2); if (MIX_F8) { d.f8 = 1; esz = 1; }
;                 if (BR_FUSE) { K = 1536; WT = ws + WS_WOA + (size_t)l * D * 1536; }
;             } else if ((r -= C_OB) < C_O) { const int kb = r / 32, nb = r % 32; n0 = 64 * nb; k0 = 64 * kb; ldw = D; K = D; scol = n0 + 4 * q4; W = a.w_out + (size_t)l * D * D; WT = ws + WS_WO + (size_t)l * D * D * (MIX_F8 ? 1 : 2); if (MIX_F8) { d.f8 = 1; esz = 1; }
;             } else if ((r -= C_O) < C_GU) { const int e = r / 1024, r2 = r % 1024, kb = r2 / 32, nb = r2 % 32, pn = nb >> 2, sgu = (nb >> 1) & 1, c0 = 64 * (nb & 1);
;                 n0 = 64 * nb; k0 = 64 * kb; ldw = FF; K = D; scol = 128 * pn + c0 + 4 * q4; W = (sgu ? a.w_up_e : a.w_gate_e) + (size_t)(l * NE + e) * D * FF; WT = ws + WS_WGU + (size_t)(l * NE + e) * 2048 * D; d.f8 = 1; esz = 1;
.LBB0_72_hp:
	s_cmp_ge_i32 s42, s101
	s_cbranch_scc1 .LBB0_70_hp
	s_lshr_b32 s44, s42, 6
	s_lshl_b32 s44, s44, 3
	s_bfe_u32 s100, s42, 0x30002
	s_or_b32 s44, s44, s100
	s_add_i32 s44, s44, s74
	s_and_b32 s100, s44, 7
	s_lshr_b32 s44, s44, 3
	s_lshl_b32 s44, s44, 6
	s_lshl_b32 s100, s100, 2
	s_or_b32 s44, s44, s100
	s_and_b32 s100, s42, 0x23
	s_or_b32 s44, s44, s100
	s_cmp_lt_i32 s44, s101
	s_cselect_b64 s[20:21], -1, 0
	s_cmp_ge_i32 s44, s101
	s_cselect_b64 s[12:13], -1, 0
	s_and_b64 vcc, exec, s[12:13]
	s_cbranch_vccnz .LBB0_106_hp
	s_sub_i32 s3, 0xfcff, s44
	s_mul_hi_u32 s0, s3, 0x81848da9
	s_lshr_b32 s0, s0, 14
	s_mul_i32 s14, s0, 0x7e80
	s_sub_i32 s45, s3, s14
	s_cmpk_gt_u32 s45, 0x177f
	s_cbranch_scc0 .LBB0_81_hp
	s_cmpk_gt_u32 s45, 0x187f
	s_cbranch_scc0 .LBB0_83_hp
	s_cmpk_gt_u32 s45, 0x1a7f
	s_cbranch_scc0 .LBB0_84_hp
	s_cmpk_gt_u32 s45, 0x1e7f
	s_cbranch_scc0 .LBB0_85_hp
	s_lshl_b32 s24, s45, 6
	s_cmpk_gt_u32 s45, 0x5e7f
	s_cbranch_scc0 .LBB0_121_hp
	s_add_i32 s14, s45, 0xffffa180
	s_lshr_b32 s18, s14, 9
	s_lshl_b32 s14, s14, 1
	s_and_b32 s49, s14, 0x3c0
	s_load_dwordx2 s[14:15], s[8:9], 0x88
	s_lshl_b32 s19, s0, 4
	s_add_i32 s22, s18, s19
	s_mov_b32 s23, s1
	s_and_b32 s3, s24, 0x7c0
	s_lshl_b64 s[18:19], s[22:23], 23
	s_waitcnt lgkmcnt(0)
	s_add_u32 s18, s14, s18
	s_addc_u32 s19, s15, s19
	s_lshl_b64 s[14:15], s[22:23], 21
	s_add_u32 s22, s28, s14
	v_or_b32_e32 v0, s3, v136
	s_addc_u32 s23, s29, s15
	s_cbranch_execz .LBB0_122_hp
	s_movk_i32 s14, 0x400
	s_mov_b64 s[24:25], 0x800
	s_cbranch_execz .LBB0_86_hp
	s_branch .LBB0_87_hp

; #define LAS __attribute__((address_space(3)))
; #define GAS __attribute__((address_space(1)))
; #define LDS_WAIT() asm volatile("s_waitcnt lgkmcnt(0)" ::: "memory")
; __device__ __forceinline__ unsigned pk_fp8x4(float a, float b, float c, float d) { int p = __builtin_amdgcn_cvt_pk_fp8_f32(sat8(a), sat8(b), 0, false); p = __builtin_amdgcn_cvt_pk_fp8_f32(sat8(c), sat8(d), p, true); return (unsigned)p; }
; __device__ __forceinline__ void tr_finish(const TrDesc& d, f32x4 (&v)[16], LAS float* scr, int lane) {
;     const int kk = lane >> 4, q4 = lane & 15;
;     if (d.zero) {
; #pragma unroll
;         for (int i = 0; i < 16; ++i) v[i] = (f32x4){0.f, 0.f, 0.f, 0.f}; }
;     const int d0 = d.rope ? 8 * (q4 & 7) + (q4 >> 3) : 4 * q4, ds = d.rope ? 2 : 1;
;     { LAS float* rp = scr + kk * 65 + d0;
; #pragma unroll
;         for (int i = 0; i < 16; ++i) { rp[4 * i * 65] = v[i][0]; rp[4 * i * 65 + ds] = v[i][1]; rp[4 * i * 65 + 2 * ds] = v[i][2]; rp[4 * i * 65 + 3 * ds] = v[i][3]; } }
;     LDS_WAIT(); asm volatile("" ::: "memory");
;     if (d.f8) {
;         const int c = lane & 3, nl = lane >> 2; const LAS float* sp = scr + (16 * c) * 65 + nl; unsigned char* dp = d.dst + (size_t)nl * d.K + 16 * c;
; #pragma unroll
;         for (int j = 0; j < 4; ++j) { u32x4 o;
;             o.x = pk_fp8x4(sp[0 * 65 + 16 * j] * 32.0f, sp[1 * 65 + 16 * j] * 32.0f, sp[2 * 65 + 16 * j] * 32.0f, sp[3 * 65 + 16 * j] * 32.0f);
;             o.y = pk_fp8x4(sp[4 * 65 + 16 * j] * 32.0f, sp[5 * 65 + 16 * j] * 32.0f, sp[6 * 65 + 16 * j] * 32.0f, sp[7 * 65 + 16 * j] * 32.0f);
;             o.z = pk_fp8x4(sp[8 * 65 + 16 * j] * 32.0f, sp[9 * 65 + 16 * j] * 32.0f, sp[10 * 65 + 16 * j] * 32.0f, sp[11 * 65 + 16 * j] * 32.0f);
;             o.w = pk_fp8x4(sp[12 * 65 + 16 * j] * 32.0f, sp[13 * 65 + 16 * j] * 32.0f, sp[14 * 65 + 16 * j] * 32.0f, sp[15 * 65 + 16 * j] * 32.0f);
;             *(GAS u32x4*)(dp + (size_t)(16 * j) * d.K) = o; }
.LBB0_108_hp:
	s_or_b64 exec, exec, s[22:23]
	s_cmp_eq_u32 s43, 0
	s_cselect_b64 vcc, -1, 0
	s_cmp_lg_u32 s43, 0
	s_cselect_b64 s[22:23], -1, 0
	v_cndmask_b32_e64 v2, 0, 1, s[22:23]
	s_and_b64 s[22:23], s[22:23], exec
	v_cndmask_b32_e32 v0, v140, v136, vcc
	s_cselect_b32 s0, 2, 1
	v_lshl_add_u32 v0, v0, 2, v141
	s_lshl_b32 s3, s0, 2
	v_add_u32_e32 v3, s3, v0
	v_lshlrev_b32_e64 v2, v2, 3
	s_waitcnt vmcnt(15)
	ds_write_b32 v3, v5
	v_lshl_add_u32 v3, s0, 3, v0
	v_lshl_add_u32 v2, v2, 2, v0
	v_subrev_u32_e32 v146, s3, v3
	ds_write_b32 v0, v4
	ds_write_b32 v3, v6
	ds_write_b32 v2, v7
	s_waitcnt vmcnt(14)
	ds_write_b32 v0, v8 offset:1040
	ds_write_b32 v146, v9 offset:1040
	ds_write_b32 v3, v10 offset:1040
	ds_write_b32 v2, v11 offset:1040
	s_waitcnt vmcnt(13)
	ds_write_b32 v0, v12 offset:2080
	ds_write_b32 v146, v13 offset:2080
	ds_write_b32 v3, v14 offset:2080
	ds_write_b32 v2, v15 offset:2080
	s_waitcnt vmcnt(12)
	ds_write_b32 v0, v16 offset:3120
	ds_write_b32 v146, v17 offset:3120
	ds_write_b32 v3, v18 offset:3120
	ds_write_b32 v2, v19 offset:3120
	s_waitcnt vmcnt(11)
	ds_write_b32 v0, v20 offset:4160
	ds_write_b32 v146, v21 offset:4160
	ds_write_b32 v3, v22 offset:4160
	ds_write_b32 v2, v23 offset:4160
	s_waitcnt vmcnt(10)
	ds_write_b32 v0, v24 offset:5200
	ds_write_b32 v146, v25 offset:5200
	ds_write_b32 v3, v26 offset:5200
	ds_write_b32 v2, v27 offset:5200
	s_waitcnt vmcnt(9)
	ds_write_b32 v0, v28 offset:6240
	ds_write_b32 v146, v29 offset:6240
	ds_write_b32 v3, v30 offset:6240
	ds_write_b32 v2, v31 offset:6240
	s_waitcnt vmcnt(8)
	ds_write_b32 v0, v32 offset:7280
	ds_write_b32 v146, v33 offset:7280
	ds_write_b32 v3, v34 offset:7280
	ds_write_b32 v2, v35 offset:7280
	s_waitcnt vmcnt(7)
	ds_write_b32 v0, v36 offset:8320
	ds_write_b32 v146, v37 offset:8320
	ds_write_b32 v3, v38 offset:8320
	ds_write_b32 v2, v39 offset:8320
	s_waitcnt vmcnt(6)
	ds_write_b32 v0, v40 offset:9360
	ds_write_b32 v146, v41 offset:9360
	ds_write_b32 v3, v42 offset:9360
	ds_write_b32 v2, v43 offset:9360
	s_waitcnt vmcnt(5)
	ds_write_b32 v0, v44 offset:10400
	ds_write_b32 v146, v45 offset:10400
	ds_write_b32 v3, v46 offset:10400
	ds_write_b32 v2, v47 offset:10400
	s_waitcnt vmcnt(4)
	ds_write_b32 v0, v48 offset:11440
	ds_write_b32 v146, v49 offset:11440
	ds_write_b32 v3, v50 offset:11440
	ds_write_b32 v2, v51 offset:11440
	s_waitcnt vmcnt(3)
	ds_write_b32 v0, v52 offset:12480
	ds_write_b32 v146, v53 offset:12480
	ds_write_b32 v3, v54 offset:12480
	ds_write_b32 v2, v55 offset:12480
	s_waitcnt vmcnt(2)
	ds_write_b32 v0, v56 offset:13520
	ds_write_b32 v146, v57 offset:13520
	ds_write_b32 v3, v58 offset:13520
	ds_write_b32 v2, v59 offset:13520
	s_waitcnt vmcnt(1)
	ds_write_b32 v0, v60 offset:14560
	ds_write_b32 v146, v61 offset:14560
	ds_write_b32 v3, v62 offset:14560
	ds_write_b32 v2, v63 offset:14560
	s_waitcnt vmcnt(0)
	ds_write_b32 v0, v64 offset:15600
	ds_write_b32 v146, v65 offset:15600
	ds_write_b32 v3, v66 offset:15600
	ds_write_b32 v2, v67 offset:15600
	s_waitcnt lgkmcnt(0)
	ds_read2_b32 v[2:3], v142 offset1:16
	ds_read2_b32 v[148:149], v142 offset0:65 offset1:81
	ds_read2_b32 v[154:155], v142 offset0:130 offset1:146
	ds_read2_b32 v[156:157], v142 offset0:195 offset1:211
	v_mov_b32_e32 v150, 0
	s_waitcnt lgkmcnt(3)
	v_mul_f32_e32 v0, 0x42000000, v2
	s_waitcnt lgkmcnt(2)
	v_mul_f32_e32 v2, 0x42000000, v148
	v_med3_f32 v0, v0, s41, v143
	s_waitcnt lgkmcnt(0)
	v_mul_f32_e32 v147, 0x42000000, v156
	v_med3_f32 v2, v2, s41, v143
	v_cvt_pk_fp8_f32 v150, v0, v2
	v_med3_f32 v2, v147, s41, v143
	v_add_u32_e32 v147, 0x400, v142
	ds_read2_b32 v[160:161], v147 offset0:4 offset1:20
	ds_read2_b32 v[162:163], v147 offset0:69 offset1:85
	ds_read2_b32 v[164:165], v147 offset0:134 offset1:150
	ds_read2_b32 v[166:167], v147 offset0:199 offset1:215
	v_mul_f32_e32 v146, 0x42000000, v154
	v_med3_f32 v0, v146, s41, v143
	v_cvt_pk_fp8_f32 v150, v0, v2 op_sel:[0,0,1]
	s_waitcnt lgkmcnt(3)
	v_mul_f32_e32 v0, 0x42000000, v160
	s_waitcnt lgkmcnt(2)
	v_mul_f32_e32 v2, 0x42000000, v162
	s_waitcnt lgkmcnt(0)
	v_mul_f32_e32 v148, 0x42000000, v166
	v_med3_f32 v0, v0, s41, v143
	v_med3_f32 v2, v2, s41, v143
	v_mov_b32_e32 v151, 0
	v_cvt_pk_fp8_f32 v151, v0, v2
	v_med3_f32 v2, v148, s41, v143
	v_add_u32_e32 v148, 0x800, v142
	ds_read2_b32 v[168:169], v148 offset0:8 offset1:24
	ds_read2_b32 v[170:171], v148 offset0:73 offset1:89
	ds_read2_b32 v[172:173], v148 offset0:138 offset1:154
	ds_read2_b32 v[174:175], v148 offset0:203 offset1:219
	v_mul_f32_e32 v146, 0x42000000, v164
	v_med3_f32 v0, v146, s41, v143
	v_cvt_pk_fp8_f32 v151, v0, v2 op_sel:[0,0,1]
	s_waitcnt lgkmcnt(3)
	v_mul_f32_e32 v0, 0x42000000, v168
	s_waitcnt lgkmcnt(2)
	v_mul_f32_e32 v2, 0x42000000, v170
	s_waitcnt lgkmcnt(1)
	v_mul_f32_e32 v146, 0x42000000, v172
	v_med3_f32 v0, v0, s41, v143
	v_med3_f32 v2, v2, s41, v143
	v_mov_b32_e32 v152, 0
	v_cvt_pk_fp8_f32 v152, v0, v2
	v_med3_f32 v0, v146, s41, v143
	v_add_u32_e32 v146, 0xc00, v142
	ds_read2_b32 v[176:177], v146 offset0:12 offset1:28
	ds_read2_b32 v[178:179], v146 offset0:77 offset1:93
	ds_read2_b32 v[180:181], v146 offset0:142 offset1:158
	s_waitcnt lgkmcnt(3)
	v_mul_f32_e32 v153, 0x42000000, v174
	v_med3_f32 v2, v153, s41, v143
	ds_read2_b32 v[182:183], v146 offset0:207 offset1:223
	v_cvt_pk_fp8_f32 v152, v0, v2 op_sel:[0,0,1]
	s_waitcnt lgkmcnt(3)
	v_mul_f32_e32 v0, 0x42000000, v176
	s_waitcnt lgkmcnt(2)
	v_mul_f32_e32 v2, 0x42000000, v178
	v_med3_f32 v0, v0, s41, v143
	v_med3_f32 v2, v2, s41, v143
	v_mov_b32_e32 v153, 0
	v_cvt_pk_fp8_f32 v153, v0, v2
	s_waitcnt lgkmcnt(1)
	v_mul_f32_e32 v154, 0x42000000, v180
	s_waitcnt lgkmcnt(0)
; #define LAS __attribute__((address_space(3)))
; #define GAS __attribute__((address_space(1)))
; __device__ __forceinline__ unsigned pk_fp8x4(float a, float b, float c, float d) { int p = __builtin_amdgcn_cvt_pk_fp8_f32(sat8(a), sat8(b), 0, false); p = __builtin_amdgcn_cvt_pk_fp8_f32(sat8(c), sat8(d), p, true); return (unsigned)p; }
; __device__ __forceinline__ void tr_finish(const TrDesc& d, f32x4 (&v)[16], LAS float* scr, int lane) {
;     ...
;     if (d.f8) {
;         const int c = lane & 3, nl = lane >> 2; const LAS float* sp = scr + (16 * c) * 65 + nl; unsigned char* dp = d.dst + (size_t)nl * d.K + 16 * c;
; #pragma unroll
;         for (int j = 0; j < 4; ++j) { u32x4 o;
;             o.x = pk_fp8x4(sp[0 * 65 + 16 * j] * 32.0f, sp[1 * 65 + 16 * j] * 32.0f, sp[2 * 65 + 16 * j] * 32.0f, sp[3 * 65 + 16 * j] * 32.0f);
;             o.y = pk_fp8x4(sp[4 * 65 + 16 * j] * 32.0f, sp[5 * 65 + 16 * j] * 32.0f, sp[6 * 65 + 16 * j] * 32.0f, sp[7 * 65 + 16 * j] * 32.0f);
;             o.z = pk_fp8x4(sp[8 * 65 + 16 * j] * 32.0f, sp[9 * 65 + 16 * j] * 32.0f, sp[10 * 65 + 16 * j] * 32.0f, sp[11 * 65 + 16 * j] * 32.0f);
;             o.w = pk_fp8x4(sp[12 * 65 + 16 * j] * 32.0f, sp[13 * 65 + 16 * j] * 32.0f, sp[14 * 65 + 16 * j] * 32.0f, sp[15 * 65 + 16 * j] * 32.0f);
;             *(GAS u32x4*)(dp + (size_t)(16 * j) * d.K) = o; }
	v_mul_f32_e32 v0, 0x42000000, v182
	v_med3_f32 v2, v154, s41, v143
	v_med3_f32 v0, v0, s41, v143
	v_cvt_pk_fp8_f32 v153, v2, v0 op_sel:[0,0,1]
	v_mov_b64_e32 v[158:159], s[16:17]
	v_mad_i64_i32 v[158:159], s[22:23], s2, v132, v[158:159]
	v_lshl_add_u64 v[158:159], v[158:159], 0, v[134:135]
	v_mul_f32_e32 v0, 0x42000000, v3
	v_mul_f32_e32 v2, 0x42000000, v149
	global_store_dwordx4 v[158:159], v[150:153], off nt
	v_med3_f32 v0, v0, s41, v143
	v_med3_f32 v2, v2, s41, v143
	v_mov_b32_e32 v150, 0
	v_cvt_pk_fp8_f32 v150, v0, v2
	v_mul_f32_e32 v3, 0x42000000, v155
	v_mul_f32_e32 v0, 0x42000000, v157
	v_med3_f32 v2, v3, s41, v143
	v_med3_f32 v0, v0, s41, v143
	v_cvt_pk_fp8_f32 v150, v2, v0 op_sel:[0,0,1]
	v_mul_f32_e32 v0, 0x42000000, v161
	v_mul_f32_e32 v2, 0x42000000, v163
	v_med3_f32 v0, v0, s41, v143
	v_med3_f32 v2, v2, s41, v143
	v_mov_b32_e32 v151, 0
	v_cvt_pk_fp8_f32 v151, v0, v2
	v_mul_f32_e32 v3, 0x42000000, v165
	v_mul_f32_e32 v0, 0x42000000, v167
	v_med3_f32 v2, v3, s41, v143
	v_med3_f32 v0, v0, s41, v143
	v_cvt_pk_fp8_f32 v151, v2, v0 op_sel:[0,0,1]
	v_mul_f32_e32 v0, 0x42000000, v169
	v_mul_f32_e32 v2, 0x42000000, v171
	v_med3_f32 v0, v0, s41, v143
	v_med3_f32 v2, v2, s41, v143
	v_mov_b32_e32 v152, 0
	v_cvt_pk_fp8_f32 v152, v0, v2
	v_mul_f32_e32 v3, 0x42000000, v173
	v_mul_f32_e32 v0, 0x42000000, v175
	v_med3_f32 v2, v3, s41, v143
	v_med3_f32 v0, v0, s41, v143
	v_cvt_pk_fp8_f32 v152, v2, v0 op_sel:[0,0,1]
	v_mul_f32_e32 v0, 0x42000000, v177
	v_mul_f32_e32 v2, 0x42000000, v179
	v_med3_f32 v0, v0, s41, v143
	v_med3_f32 v2, v2, s41, v143
	v_mov_b32_e32 v153, 0
	v_cvt_pk_fp8_f32 v153, v0, v2
	s_ashr_i32 s3, s2, 31
	v_mul_f32_e32 v3, 0x42000000, v181
	v_mul_f32_e32 v0, 0x42000000, v183
	v_med3_f32 v2, v3, s41, v143
	v_med3_f32 v0, v0, s41, v143
	s_lshl_b64 s[22:23], s[2:3], 4
	v_cvt_pk_fp8_f32 v153, v2, v0 op_sel:[0,0,1]
	v_lshl_add_u64 v[2:3], v[158:159], 0, s[22:23]
	ds_read2_b32 v[154:155], v142 offset0:32 offset1:48
	ds_read2_b32 v[156:157], v142 offset0:97 offset1:113
	ds_read2_b32 v[158:159], v142 offset0:162 offset1:178
	ds_read2_b32 v[160:161], v142 offset0:227 offset1:243
	s_andn2_b64 vcc, exec, s[20:21]
	s_waitcnt lgkmcnt(3)
	v_mul_f32_e32 v0, 0x42000000, v154
	s_waitcnt lgkmcnt(2)
	v_mul_f32_e32 v149, 0x42000000, v156
	global_store_dwordx4 v[2:3], v[150:153], off nt
	v_med3_f32 v0, v0, s41, v143
	v_med3_f32 v149, v149, s41, v143
	v_mov_b32_e32 v150, 0
	v_cvt_pk_fp8_f32 v150, v0, v149
	ds_read2_b32 v[162:163], v147 offset0:36 offset1:52
	ds_read2_b32 v[164:165], v147 offset0:101 offset1:117
	ds_read2_b32 v[166:167], v147 offset0:166 offset1:182
	ds_read2_b32 v[168:169], v147 offset0:231 offset1:247
	s_waitcnt lgkmcnt(5)
	v_mul_f32_e32 v151, 0x42000000, v158
	s_waitcnt lgkmcnt(4)
	v_mul_f32_e32 v152, 0x42000000, v160
	v_med3_f32 v0, v151, s41, v143
	v_med3_f32 v149, v152, s41, v143
	v_cvt_pk_fp8_f32 v150, v0, v149 op_sel:[0,0,1]
	s_waitcnt lgkmcnt(3)
	v_mul_f32_e32 v0, 0x42000000, v162
	s_waitcnt lgkmcnt(2)
	v_mul_f32_e32 v149, 0x42000000, v164
	v_med3_f32 v0, v0, s41, v143
	v_med3_f32 v149, v149, s41, v143
	v_mov_b32_e32 v151, 0
	v_cvt_pk_fp8_f32 v151, v0, v149
	ds_read2_b32 v[170:171], v148 offset0:40 offset1:56
	ds_read2_b32 v[172:173], v148 offset0:105 offset1:121
	ds_read2_b32 v[174:175], v148 offset0:170 offset1:186
	ds_read2_b32 v[176:177], v148 offset0:235 offset1:251
	s_waitcnt lgkmcnt(5)
	v_mul_f32_e32 v152, 0x42000000, v166
	s_waitcnt lgkmcnt(4)
	v_mul_f32_e32 v153, 0x42000000, v168
	v_med3_f32 v0, v152, s41, v143
	v_med3_f32 v149, v153, s41, v143
	v_cvt_pk_fp8_f32 v151, v0, v149 op_sel:[0,0,1]
	s_waitcnt lgkmcnt(3)
	v_mul_f32_e32 v0, 0x42000000, v170
	s_waitcnt lgkmcnt(2)
	v_mul_f32_e32 v149, 0x42000000, v172
	v_med3_f32 v0, v0, s41, v143
	v_med3_f32 v149, v149, s41, v143
	v_mov_b32_e32 v152, 0
	v_cvt_pk_fp8_f32 v152, v0, v149
	ds_read2_b32 v[178:179], v146 offset0:44 offset1:60
	ds_read2_b32 v[180:181], v146 offset0:109 offset1:125
	ds_read2_b32 v[182:183], v146 offset0:174 offset1:190
	s_waitcnt lgkmcnt(4)
	v_mul_f32_e32 v153, 0x42000000, v174
	s_waitcnt lgkmcnt(3)
	v_mul_f32_e32 v154, 0x42000000, v176
	v_med3_f32 v0, v153, s41, v143
	v_med3_f32 v149, v154, s41, v143
	ds_read2_b32 v[184:185], v146 offset0:239 offset1:255
	v_cvt_pk_fp8_f32 v152, v0, v149 op_sel:[0,0,1]
	s_waitcnt lgkmcnt(3)
	v_mul_f32_e32 v0, 0x42000000, v178
	s_waitcnt lgkmcnt(2)
	v_mul_f32_e32 v149, 0x42000000, v180
	v_med3_f32 v0, v0, s41, v143
	v_med3_f32 v149, v149, s41, v143
	v_mov_b32_e32 v153, 0
	v_cvt_pk_fp8_f32 v153, v0, v149
	s_waitcnt lgkmcnt(1)
	v_mul_f32_e32 v154, 0x42000000, v182
	s_waitcnt lgkmcnt(0)
	v_mul_f32_e32 v0, 0x42000000, v184
	v_med3_f32 v149, v154, s41, v143
	v_med3_f32 v0, v0, s41, v143
	v_cvt_pk_fp8_f32 v153, v149, v0 op_sel:[0,0,1]
	v_mul_f32_e32 v0, 0x42000000, v155
	v_mul_f32_e32 v149, 0x42000000, v157
	v_med3_f32 v0, v0, s41, v143
	v_med3_f32 v149, v149, s41, v143
	v_mov_b32_e32 v154, 0
	v_cvt_pk_fp8_f32 v154, v0, v149
	v_mul_f32_e32 v155, 0x42000000, v159
	v_mul_f32_e32 v0, 0x42000000, v161
	v_med3_f32 v149, v155, s41, v143
	v_med3_f32 v0, v0, s41, v143
	v_cvt_pk_fp8_f32 v154, v149, v0 op_sel:[0,0,1]
	v_mul_f32_e32 v0, 0x42000000, v163
	v_mul_f32_e32 v149, 0x42000000, v165
	v_med3_f32 v0, v0, s41, v143
	v_med3_f32 v149, v149, s41, v143
	v_mov_b32_e32 v155, 0
	v_cvt_pk_fp8_f32 v155, v0, v149
	v_mul_f32_e32 v156, 0x42000000, v167
	v_mul_f32_e32 v0, 0x42000000, v169
	v_med3_f32 v149, v156, s41, v143
	v_med3_f32 v0, v0, s41, v143
	v_cvt_pk_fp8_f32 v155, v149, v0 op_sel:[0,0,1]
	v_mul_f32_e32 v0, 0x42000000, v171
	v_mul_f32_e32 v149, 0x42000000, v173
	v_med3_f32 v0, v0, s41, v143
	v_med3_f32 v149, v149, s41, v143
	v_mov_b32_e32 v156, 0
	v_cvt_pk_fp8_f32 v156, v0, v149
	v_mul_f32_e32 v157, 0x42000000, v175
	v_mul_f32_e32 v0, 0x42000000, v177
	v_med3_f32 v149, v157, s41, v143
	v_med3_f32 v0, v0, s41, v143
	v_cvt_pk_fp8_f32 v156, v149, v0 op_sel:[0,0,1]
	v_mul_f32_e32 v0, 0x42000000, v179
	v_mul_f32_e32 v149, 0x42000000, v181
	v_med3_f32 v0, v0, s41, v143
	v_med3_f32 v149, v149, s41, v143
	v_mov_b32_e32 v157, 0
	v_cvt_pk_fp8_f32 v157, v0, v149
	v_mul_f32_e32 v158, 0x42000000, v183
	v_mul_f32_e32 v0, 0x42000000, v185
	v_med3_f32 v149, v158, s41, v143
	v_med3_f32 v0, v0, s41, v143
	v_cvt_pk_fp8_f32 v157, v149, v0 op_sel:[0,0,1]
	v_lshl_add_u64 v[2:3], v[2:3], 0, s[22:23]
	global_store_dwordx4 v[2:3], v[150:153], off nt
	v_lshl_add_u64 v[2:3], v[2:3], 0, s[22:23]
	global_store_dwordx4 v[2:3], v[154:157], off nt
	s_waitcnt lgkmcnt(0)
	s_cbranch_vccnz .LBB0_71_hp
;     ...
;         auto decode = [&](int it) -> TrDesc {
;             TrDesc d; d.zero = 0; d.rope = 0; d.f8 = 0;
;             const int l = it / C_L; int r = it % C_L;
;             const float* W; unsigned char* WT; int ldw, K, k0, n0, scol, esz = 2;
;             if (r < C_IN) { const int kb = r / 188, nb = r % 188; n0 = 64 * nb; k0 = 64 * kb; ldw = NIN; K = D; W = a.w_in + (size_t)l * D * NIN;
;                 if (n0 < 3072) { d.rope = 1; scol = (n0 >> 7) * 128 + 32 * ((n0 >> 6) & 1) + 64 * (q4 >> 3) + 4 * (q4 & 7); }
;                 else if (n0 < 7680) scol = n0 + 4 * q4;
;                 else if (n0 < 11776) scol = n0 + 16 + 4 * q4;
;                 else if (n0 == 11776) { scol = (q4 < 4) ? 7680 + 4 * q4 : 0; d.zero = (q4 < 4) ? 0 : 1; }
;                 else { scol = 0; d.zero = 1; }
;     ...
;                 d.f8 = 1; esz = 1; WT = ws + WS_WIN + (size_t)l * NP * D;
;     ...
;                 WT = ws + WS_WIN + (size_t)l * NP * D * 2;
;     ...
;             } else if ((r -= C_IN) < C_OA) { const int kb = r / 32, nb = r % 32; n0 = 64 * nb; k0 = 64 * kb; ldw = D; K = 512; scol = n0 + 4 * q4; W = a.w_out_a + (size_t)l * 512 * D; WT = ws + WS_WOA + (size_t)l * D * 512 * (MIX_F8 ? 1 : 2); if (MIX_F8) { d.f8 = 1; esz = 1; }
;                 if (BR_FUSE) { K = 1536; WT = ws + WS_WOA + (size_t)l * D * 1536 + 1024; }
;             } else if ((r -= C_OA) < C_OB) { const int kb = r / 32, nb = r % 32; n0 = 64 * nb; k0 = 64 * kb; ldw = D; K = 1024; scol = n0 + 4 * q4; W = a.w_out_b + (size_t)l * 1024 * D; WT = ws + WS_WOB + (size_t)l * D * 1024 * (MIX_F8 ? 1 : 2); if (MIX_F8) { d.f8 = 1; esz = 1; }
;                 if (BR_FUSE) { K = 1536; WT = ws + WS_WOA + (size_t)l * D * 1536; }
;             } else if ((r -= C_OB) < C_O) { const int kb = r / 32, nb = r % 32; n0 = 64 * nb; k0 = 64 * kb; ldw = D; K = D; scol = n0 + 4 * q4; W = a.w_out + (size_t)l * D * D; WT = ws + WS_WO + (size_t)l * D * D * (MIX_F8 ? 1 : 2); if (MIX_F8) { d.f8 = 1; esz = 1; }
;     ...
;         while (it < NIT) {
;             const int itB = it + NGW;
;             if (itB < NIT) { dB = decode(NIT - 1 - itB); tr_load(dB, vB); }
;             tr_finish(dA, vA, scr, lane);
;             if (itB >= NIT) break;
;             const int itA = itB + NGW;
;             if (itA < NIT) { dA = decode(NIT - 1 - itA); tr_load(dA, vA); }
;             tr_finish(dB, vB, scr, lane);
;             it = itA;
	s_lshr_b32 s42, s44, 6
	s_lshl_b32 s42, s42, 3
	s_bfe_u32 s100, s44, 0x30002
	s_or_b32 s42, s42, s100
	s_add_i32 s42, s42, s74
	s_and_b32 s100, s42, 7
	s_lshr_b32 s42, s42, 3
	s_lshl_b32 s42, s42, 6
	s_lshl_b32 s100, s100, 2
	s_or_b32 s42, s42, s100
	s_and_b32 s100, s44, 0x23
	s_or_b32 s42, s42, s100
	s_cmp_ge_i32 s42, s101
	s_cbranch_scc1 .LBB0_144_hp
	s_sub_i32 s2, 0xfcff, s42
	s_mul_hi_u32 s0, s2, 0x81848da9
	s_lshr_b32 s0, s0, 14
	s_mul_i32 s3, s0, 0x7e80
	s_sub_i32 s27, s2, s3
	s_cmpk_gt_u32 s27, 0x177f
	s_cbranch_scc0 .LBB0_117_hp
	s_cmpk_gt_u32 s27, 0x187f
	s_cbranch_scc0 .LBB0_119_hp
	s_cmpk_gt_u32 s27, 0x1a7f
	s_cbranch_scc0 .LBB0_120_hp
	s_cmpk_gt_u32 s27, 0x1e7f
	s_cbranch_scc0 .LBB0_123_hp
	s_lshl_b32 s22, s27, 6
	s_cmpk_gt_u32 s27, 0x5e7f
	s_cbranch_scc0 .LBB0_147_hp
	s_add_i32 s2, s27, 0xffffa180
	s_lshr_b32 s16, s2, 9
	s_lshl_b32 s2, s2, 1
	s_and_b32 s44, s2, 0x3c0
	s_load_dwordx2 s[2:3], s[8:9], 0x88
	s_lshl_b32 s17, s0, 4
	s_add_i32 s20, s16, s17
	s_mov_b32 s21, s1
	s_and_b32 s15, s22, 0x7c0
	s_lshl_b64 s[16:17], s[20:21], 23
	s_waitcnt lgkmcnt(0)
	s_add_u32 s16, s2, s16
	s_addc_u32 s17, s3, s17
	s_lshl_b64 s[2:3], s[20:21], 21
	s_add_u32 s20, s28, s2
	v_or_b32_e32 v0, s15, v136
	s_addc_u32 s21, s29, s3
	s_cbranch_execz .LBB0_148_hp
	s_movk_i32 s2, 0x400
	s_mov_b64 s[22:23], 0x800
	s_cbranch_execz .LBB0_124_hp
	s_branch .LBB0_125_hp
